# P6 output-gate bytes loaded as 4 coalesced 16-byte loads per lane plus a 4x4 lane transpose (v_permlane32/16_swap) instead of 16 scattered dword loads
# speedup vs baseline: 1.0245x; 1.0010x over previous
.LBB0_764:
	v_permlane32_swap_b32_e32 v204, v206
	v_permlane32_swap_b32_e32 v205, v207
	v_permlane32_swap_b32_e32 v208, v210
	v_permlane32_swap_b32_e32 v209, v211
	v_permlane32_swap_b32_e32 v212, v214
	v_permlane32_swap_b32_e32 v213, v215
	v_permlane32_swap_b32_e32 v202, v216
	v_permlane32_swap_b32_e32 v203, v217
	v_permlane16_swap_b32_e32 v204, v205
	v_permlane16_swap_b32_e32 v206, v207
	v_permlane16_swap_b32_e32 v208, v209
	v_permlane16_swap_b32_e32 v210, v211
	v_permlane16_swap_b32_e32 v212, v213
	v_permlane16_swap_b32_e32 v214, v215
	v_permlane16_swap_b32_e32 v202, v203
	v_permlane16_swap_b32_e32 v216, v217
	s_nop 1
	v_mov_b32_e32 v201, v211
	v_mov_b32_e32 v105, v212
	v_mov_b32_e32 v211, v230
	v_ashrrev_i32_e32 v212, 4, v211
	v_mul_f32_e32 v2, v177, v177
	v_mul_f32_e32 v3, v179, v179
	v_fmac_f32_e32 v2, v176, v176
	v_fmac_f32_e32 v3, v178, v178
	v_add_f32_e32 v2, v2, v3
	v_mul_f32_e32 v3, v175, v175
	v_mul_f32_e32 v4, v173, v173
	v_fmac_f32_e32 v3, v174, v174
	v_fmac_f32_e32 v4, v172, v172
	v_add_f32_e32 v3, v3, v4
	v_add_f32_e32 v2, v2, v3
	v_mul_f32_e32 v3, v171, v171
	v_mul_f32_e32 v4, v169, v169
	v_fmac_f32_e32 v3, v170, v170
	v_fmac_f32_e32 v4, v168, v168
	v_add_f32_e32 v3, v3, v4
	v_add_f32_e32 v2, v2, v3
	v_mul_f32_e32 v3, v165, v165
	v_mul_f32_e32 v4, v163, v163
	v_fmac_f32_e32 v3, v164, v164
	v_fmac_f32_e32 v4, v162, v162
	v_add_f32_e32 v3, v3, v4
	v_add_f32_e32 v2, v2, v3
	v_mul_f32_e32 v3, v161, v161
	v_mul_f32_e32 v4, v159, v159
	v_fmac_f32_e32 v3, v160, v160
	v_fmac_f32_e32 v4, v158, v158
	v_add_f32_e32 v3, v3, v4
	v_add_f32_e32 v2, v2, v3
	v_mul_f32_e32 v3, v157, v157
	v_mul_f32_e32 v4, v155, v155
	v_fmac_f32_e32 v3, v156, v156
	v_fmac_f32_e32 v4, v154, v154
	v_add_f32_e32 v3, v3, v4
	v_add_f32_e32 v2, v2, v3
	v_mul_f32_e32 v3, v153, v153
	v_mul_f32_e32 v4, v151, v151
	v_fmac_f32_e32 v3, v152, v152
	v_fmac_f32_e32 v4, v150, v150
	v_add_f32_e32 v3, v3, v4
	v_add_f32_e32 v2, v2, v3
	v_mul_f32_e32 v3, v149, v149
	v_mul_f32_e32 v4, v147, v147
	v_fmac_f32_e32 v3, v148, v148
	v_fmac_f32_e32 v4, v146, v146
	v_add_f32_e32 v3, v3, v4
	v_add_f32_e32 v2, v2, v3
	v_mul_f32_e32 v3, v145, v145
	v_mul_f32_e32 v4, v143, v143
	v_fmac_f32_e32 v3, v144, v144
	v_fmac_f32_e32 v4, v142, v142
	v_add_f32_e32 v3, v3, v4
	v_add_f32_e32 v2, v2, v3
	v_mul_f32_e32 v3, v141, v141
	v_mul_f32_e32 v4, v139, v139
	v_fmac_f32_e32 v3, v140, v140
	v_fmac_f32_e32 v4, v138, v138
	v_add_f32_e32 v3, v3, v4
	v_add_f32_e32 v2, v2, v3
	v_mul_f32_e32 v3, v137, v137
	v_mul_f32_e32 v4, v135, v135
	v_fmac_f32_e32 v3, v136, v136
	v_fmac_f32_e32 v4, v134, v134
	v_add_f32_e32 v3, v3, v4
	v_add_f32_e32 v2, v2, v3
	v_mul_f32_e32 v3, v133, v133
	v_mul_f32_e32 v4, v131, v131
	v_fmac_f32_e32 v3, v132, v132
	v_fmac_f32_e32 v4, v130, v130
	v_add_f32_e32 v3, v3, v4
	v_add_f32_e32 v2, v2, v3
	v_mul_f32_e32 v3, v129, v129
	v_mul_f32_e32 v4, v127, v127
	v_fmac_f32_e32 v3, v128, v128
	v_fmac_f32_e32 v4, v126, v126
	v_add_f32_e32 v3, v3, v4
	v_add_f32_e32 v2, v2, v3
	v_mul_f32_e32 v3, v125, v125
	v_mul_f32_e32 v4, v123, v123
	v_fmac_f32_e32 v3, v124, v124
	v_fmac_f32_e32 v4, v122, v122
	v_add_f32_e32 v3, v3, v4
	v_add_f32_e32 v2, v2, v3
	v_mul_f32_e32 v3, v121, v121
	v_mul_f32_e32 v4, v119, v119
	v_fmac_f32_e32 v3, v120, v120
	v_fmac_f32_e32 v4, v118, v118
	v_add_f32_e32 v3, v3, v4
	v_add_f32_e32 v2, v2, v3
	v_mul_f32_e32 v3, v117, v117
	v_mul_f32_e32 v4, v115, v115
	v_fmac_f32_e32 v3, v116, v116
	v_fmac_f32_e32 v4, v114, v114
	v_add_f32_e32 v3, v3, v4
	v_and_b32_e32 v4, 64, v187
	v_add_f32_e32 v2, v2, v3
	v_xor_b32_e32 v3, 16, v187
	v_add_u32_e32 v4, 64, v4
	v_cmp_lt_i32_e32 vcc, v3, v4
	v_cvt_pk_f32_fp8_e32 v[10:11], v204
	v_cvt_pk_f32_fp8_sdwa v[12:13], v204 src0_sel:WORD_1
	v_cndmask_b32_e32 v3, v187, v3, vcc
	v_lshlrev_b32_e32 v3, 2, v3
	ds_bpermute_b32 v3, v3, v2
	v_mul_f32_e32 v10, 0x3d800000, v10
	v_mul_f32_e32 v10, 0xbfb8aa3b, v10
	v_exp_f32_e32 v10, v10
	v_mul_f32_e32 v11, 0x3d800000, v11
	s_waitcnt lgkmcnt(0)
	v_add_f32_e32 v2, v2, v3
	v_xor_b32_e32 v3, 32, v187
	v_cmp_lt_i32_e32 vcc, v3, v4
	v_mul_f32_e32 v11, 0xbfb8aa3b, v11
	v_exp_f32_e32 v11, v11
	v_cndmask_b32_e32 v3, v187, v3, vcc
	v_lshlrev_b32_e32 v3, 2, v3
	ds_bpermute_b32 v3, v3, v2
	v_add_f32_e32 v10, 1.0, v10
	v_rcp_f32_e32 v10, v10
	v_add_f32_e32 v11, 1.0, v11
	v_rcp_f32_e32 v11, v11
	s_waitcnt lgkmcnt(0)
	v_add_f32_e32 v2, v2, v3
	v_fmamk_f32 v2, v2, 0x3b800000, v227
	v_mul_f32_e32 v3, 0x4f800000, v2
	v_cmp_gt_f32_e32 vcc, s78, v2
	v_and_b32_e32 v16, 16, v211
	s_nop 0
	v_cndmask_b32_e32 v2, v2, v3, vcc
	v_sqrt_f32_e32 v3, v2
	s_nop 0
	v_add_u32_e32 v4, -1, v3
	v_fma_f32 v5, -v4, v3, v2
	v_cmp_ge_f32_e64 s[0:1], 0, v5
	v_add_u32_e32 v5, 1, v3
	s_nop 0
	v_cndmask_b32_e64 v4, v3, v4, s[0:1]
	v_fma_f32 v3, -v5, v3, v2
	v_cmp_lt_f32_e64 s[0:1], 0, v3
	s_nop 1
	v_cndmask_b32_e64 v3, v4, v5, s[0:1]
	v_mul_f32_e32 v4, 0x37800000, v3
	v_cndmask_b32_e32 v3, v3, v4, vcc
	v_cmp_class_f32_e32 vcc, v2, v228
	s_nop 1
	v_cndmask_b32_e32 v2, v3, v2, vcc
	v_div_scale_f32 v3, s[0:1], v2, v2, 1.0
	v_rcp_f32_e32 v4, v3
	s_lshl_b32 s0, s16, 1
	s_add_u32 s0, s55, s0
	s_addc_u32 s1, s56, 0
	v_fma_f32 v5, -v3, v4, 1.0
	v_fmac_f32_e32 v4, v5, v4
	v_div_scale_f32 v5, vcc, 1.0, v2, 1.0
	v_mul_f32_e32 v6, v5, v4
	v_fma_f32 v7, -v3, v6, v5
	v_fmac_f32_e32 v6, v7, v4
	v_fma_f32 v3, -v3, v6, v5
	v_div_fmas_f32 v3, v3, v4, v6
	v_div_fixup_f32 v4, v3, v2, 1.0
	v_and_b32_e32 v2, -16, v211
	v_add_u32_e32 v2, 0, v2
	v_add_u32_e32 v5, 0x19000, v2
	v_lshlrev_b64 v[2:3], 12, v[166:167]
	v_lshlrev_b32_e32 v6, 2, v212
	v_lshl_add_u64 v[2:3], s[0:1], 0, v[2:3]
	v_and_b32_e32 v6, -8, v6
	v_mov_b32_e32 v7, v87
	v_lshl_add_u64 v[2:3], v[6:7], 1, v[2:3]
	ds_read_b128 v[6:9], v5
	v_mul_f32_e32 v14, v176, v4
	v_mul_f32_e32 v17, v174, v4
	s_add_i32 s79, s79, s33
	s_cmpk_gt_i32 s79, 0x1ff
	s_waitcnt lgkmcnt(0)
	v_mul_f32_e32 v6, v6, v14
	v_mul_f32_e32 v6, v10, v6
	v_mul_f32_e32 v10, v177, v4
	v_mul_f32_e32 v7, v7, v10
	v_mul_f32_e32 v7, v11, v7
	v_mul_f32_e32 v11, 0x3d800000, v12
	v_mul_f32_e32 v12, 0x3d800000, v13
	v_mul_f32_e32 v12, 0xbfb8aa3b, v12
	v_mul_f32_e32 v11, 0xbfb8aa3b, v11
	v_exp_f32_e32 v12, v12
	v_exp_f32_e32 v11, v11
	v_mul_f32_e32 v10, v178, v4
	v_mul_f32_e32 v8, v8, v10
	v_add_f32_e32 v10, 1.0, v12
	v_cvt_pk_f32_fp8_e32 v[12:13], v205
	v_add_f32_e32 v11, 1.0, v11
	v_rcp_f32_e32 v11, v11
	v_rcp_f32_e32 v10, v10
	v_mul_f32_e32 v12, 0x3d800000, v12
	v_mul_f32_e32 v12, 0xbfb8aa3b, v12
	v_mul_f32_e32 v8, v8, v11
	v_mul_f32_e32 v11, v179, v4
	v_exp_f32_e32 v12, v12
	v_mul_f32_e32 v13, 0x3d800000, v13
	v_mul_f32_e32 v9, v9, v11
	v_mul_f32_e32 v13, 0xbfb8aa3b, v13
	v_mul_f32_e32 v9, v9, v10
	v_exp_f32_e32 v13, v13
	v_cvt_pk_bf16_f32 v6, v6, v7
	v_cvt_pk_bf16_f32 v7, v8, v9
	ds_read_b128 v[8:11], v5 offset:64
	v_add_f32_e32 v12, 1.0, v12
	v_rcp_f32_e32 v12, v12
	v_add_f32_e32 v13, 1.0, v13
	v_cvt_pk_f32_fp8_sdwa v[14:15], v205 src0_sel:WORD_1
	v_rcp_f32_e32 v13, v13
	s_waitcnt lgkmcnt(0)
	v_mul_f32_e32 v8, v17, v8
	v_mul_f32_e32 v8, v8, v12
	v_mul_f32_e32 v12, v175, v4
	v_mul_f32_e32 v9, v12, v9
	v_mul_f32_e32 v9, v9, v13
	v_mul_f32_e32 v13, 0x3d800000, v14
	v_mul_f32_e32 v13, 0xbfb8aa3b, v13
	v_exp_f32_e32 v13, v13
	v_mul_f32_e32 v14, 0x3d800000, v15
	v_mul_f32_e32 v14, 0xbfb8aa3b, v14
	v_exp_f32_e32 v14, v14
	v_add_f32_e32 v13, 1.0, v13
	v_mul_f32_e32 v12, v172, v4
	v_rcp_f32_e32 v13, v13
	v_mul_f32_e32 v10, v12, v10
	v_add_f32_e32 v12, 1.0, v14
	v_rcp_f32_e32 v12, v12
	v_mul_f32_e32 v10, v10, v13
	v_mul_f32_e32 v13, v173, v4
	v_mul_f32_e32 v11, v13, v11
	v_mul_f32_e32 v11, v11, v12
	v_cvt_pk_bf16_f32 v8, v8, v9
	v_cvt_pk_bf16_f32 v9, v10, v11
	v_lshlrev_b32_e32 v10, 1, v16
	v_mov_b32_e32 v11, v87
	v_lshl_add_u64 v[2:3], v[2:3], 0, v[10:11]
	v_cvt_pk_f32_fp8_e32 v[10:11], v206
	v_permlane16_swap_b32_e32 v6, v8
	v_permlane16_swap_b32_e32 v7, v9
	v_mul_f32_e32 v10, 0x3d800000, v10
	v_mul_f32_e32 v10, 0xbfb8aa3b, v10
	v_exp_f32_e32 v10, v10
	v_mul_f32_e32 v11, 0x3d800000, v11
	v_mul_f32_e32 v11, 0xbfb8aa3b, v11
	v_exp_f32_e32 v11, v11
	global_store_dwordx4 v[2:3], v[6:9], off
	ds_read_b128 v[6:9], v5 offset:128
	v_add_f32_e32 v10, 1.0, v10
	v_rcp_f32_e32 v10, v10
	v_add_f32_e32 v11, 1.0, v11
	v_cvt_pk_f32_fp8_sdwa v[12:13], v206 src0_sel:WORD_1
	v_mul_f32_e32 v14, v170, v4
	v_rcp_f32_e32 v11, v11
	s_waitcnt lgkmcnt(0)
	v_mul_f32_e32 v6, v14, v6
	v_mul_f32_e32 v6, v6, v10
	v_mul_f32_e32 v10, v171, v4
	v_mul_f32_e32 v7, v10, v7
	v_mul_f32_e32 v7, v7, v11
	v_mul_f32_e32 v11, 0x3d800000, v12
	v_mul_f32_e32 v12, 0x3d800000, v13
	v_mul_f32_e32 v12, 0xbfb8aa3b, v12
	v_mul_f32_e32 v11, 0xbfb8aa3b, v11
	v_exp_f32_e32 v12, v12
	v_exp_f32_e32 v11, v11
	v_mul_f32_e32 v10, v168, v4
	v_mul_f32_e32 v8, v10, v8
	v_add_f32_e32 v10, 1.0, v12
	v_cvt_pk_f32_fp8_e32 v[12:13], v207
	v_add_f32_e32 v11, 1.0, v11
	v_rcp_f32_e32 v11, v11
	v_rcp_f32_e32 v10, v10
	v_mul_f32_e32 v12, 0x3d800000, v12
	v_mul_f32_e32 v12, 0xbfb8aa3b, v12
	v_mul_f32_e32 v8, v8, v11
	v_mul_f32_e32 v11, v169, v4
	v_exp_f32_e32 v12, v12
	v_mul_f32_e32 v13, 0x3d800000, v13
	v_mul_f32_e32 v9, v11, v9
	v_mul_f32_e32 v13, 0xbfb8aa3b, v13
	v_mul_f32_e32 v9, v9, v10
	v_exp_f32_e32 v13, v13
	v_cvt_pk_bf16_f32 v6, v6, v7
	v_cvt_pk_bf16_f32 v7, v8, v9
	ds_read_b128 v[8:11], v5 offset:192
	v_add_f32_e32 v12, 1.0, v12
	v_rcp_f32_e32 v12, v12
	v_add_f32_e32 v13, 1.0, v13
	v_cvt_pk_f32_fp8_sdwa v[14:15], v207 src0_sel:WORD_1
	v_mul_f32_e32 v16, v164, v4
	v_rcp_f32_e32 v13, v13
	s_waitcnt lgkmcnt(0)
	v_mul_f32_e32 v8, v16, v8
	v_mul_f32_e32 v8, v8, v12
	v_mul_f32_e32 v12, v165, v4
	v_mul_f32_e32 v9, v12, v9
	v_mul_f32_e32 v9, v9, v13
	v_mul_f32_e32 v13, 0x3d800000, v14
	v_mul_f32_e32 v13, 0xbfb8aa3b, v13
	v_exp_f32_e32 v13, v13
	v_mul_f32_e32 v14, 0x3d800000, v15
	v_mul_f32_e32 v14, 0xbfb8aa3b, v14
	v_exp_f32_e32 v14, v14
	v_add_f32_e32 v13, 1.0, v13
	v_mul_f32_e32 v12, v162, v4
	v_rcp_f32_e32 v13, v13
	v_mul_f32_e32 v10, v12, v10
	v_add_f32_e32 v12, 1.0, v14
	v_rcp_f32_e32 v12, v12
	v_mul_f32_e32 v10, v10, v13
	v_mul_f32_e32 v13, v163, v4
	v_mul_f32_e32 v11, v13, v11
	v_mul_f32_e32 v11, v11, v12
	v_cvt_pk_bf16_f32 v8, v8, v9
	v_cvt_pk_bf16_f32 v9, v10, v11
	v_cvt_pk_f32_fp8_e32 v[10:11], v208
	v_permlane16_swap_b32_e32 v6, v8
	v_permlane16_swap_b32_e32 v7, v9
	v_mul_f32_e32 v10, 0x3d800000, v10
	v_mul_f32_e32 v10, 0xbfb8aa3b, v10
	v_exp_f32_e32 v10, v10
	v_mul_f32_e32 v11, 0x3d800000, v11
	v_mul_f32_e32 v11, 0xbfb8aa3b, v11
	v_exp_f32_e32 v11, v11
	global_store_dwordx4 v[2:3], v[6:9], off offset:64
	ds_read_b128 v[6:9], v5 offset:256
	v_add_f32_e32 v10, 1.0, v10
	v_rcp_f32_e32 v10, v10
	v_add_f32_e32 v11, 1.0, v11
	v_cvt_pk_f32_fp8_sdwa v[12:13], v208 src0_sel:WORD_1
	v_mul_f32_e32 v14, v160, v4
	v_rcp_f32_e32 v11, v11
	s_waitcnt lgkmcnt(0)
	v_mul_f32_e32 v6, v14, v6
	v_mul_f32_e32 v6, v6, v10
	v_mul_f32_e32 v10, v161, v4
	v_mul_f32_e32 v7, v10, v7
	v_mul_f32_e32 v7, v7, v11
	v_mul_f32_e32 v11, 0x3d800000, v12
	v_mul_f32_e32 v12, 0x3d800000, v13
	v_mul_f32_e32 v12, 0xbfb8aa3b, v12
	v_mul_f32_e32 v11, 0xbfb8aa3b, v11
	v_exp_f32_e32 v12, v12
	v_exp_f32_e32 v11, v11
	v_mul_f32_e32 v10, v158, v4
	v_mul_f32_e32 v8, v10, v8
	v_add_f32_e32 v10, 1.0, v12
	v_cvt_pk_f32_fp8_e32 v[12:13], v209
	v_add_f32_e32 v11, 1.0, v11
	v_rcp_f32_e32 v11, v11
	v_rcp_f32_e32 v10, v10
	v_mul_f32_e32 v12, 0x3d800000, v12
	v_mul_f32_e32 v12, 0xbfb8aa3b, v12
	v_mul_f32_e32 v8, v8, v11
	v_mul_f32_e32 v11, v159, v4
	v_exp_f32_e32 v12, v12
	v_mul_f32_e32 v13, 0x3d800000, v13
	v_mul_f32_e32 v9, v11, v9
	v_mul_f32_e32 v13, 0xbfb8aa3b, v13
	v_mul_f32_e32 v9, v9, v10
	v_exp_f32_e32 v13, v13
	v_cvt_pk_bf16_f32 v6, v6, v7
	v_cvt_pk_bf16_f32 v7, v8, v9
	ds_read_b128 v[8:11], v5 offset:320
	v_add_f32_e32 v12, 1.0, v12
	v_rcp_f32_e32 v12, v12
	v_add_f32_e32 v13, 1.0, v13
	v_cvt_pk_f32_fp8_sdwa v[14:15], v209 src0_sel:WORD_1
	v_mul_f32_e32 v16, v156, v4
	v_rcp_f32_e32 v13, v13
	s_waitcnt lgkmcnt(0)
	v_mul_f32_e32 v8, v16, v8
	v_mul_f32_e32 v8, v8, v12
	v_mul_f32_e32 v12, v157, v4
	v_mul_f32_e32 v9, v12, v9
	v_mul_f32_e32 v9, v9, v13
	v_mul_f32_e32 v13, 0x3d800000, v14
	v_mul_f32_e32 v13, 0xbfb8aa3b, v13
	v_exp_f32_e32 v13, v13
	v_mul_f32_e32 v14, 0x3d800000, v15
	v_mul_f32_e32 v14, 0xbfb8aa3b, v14
	v_exp_f32_e32 v14, v14
	v_add_f32_e32 v13, 1.0, v13
	v_mul_f32_e32 v12, v154, v4
	v_rcp_f32_e32 v13, v13
	v_mul_f32_e32 v10, v12, v10
	v_add_f32_e32 v12, 1.0, v14
	v_rcp_f32_e32 v12, v12
	v_mul_f32_e32 v10, v10, v13
	v_mul_f32_e32 v13, v155, v4
	v_mul_f32_e32 v11, v13, v11
	v_mul_f32_e32 v11, v11, v12
	v_cvt_pk_bf16_f32 v8, v8, v9
	v_cvt_pk_bf16_f32 v9, v10, v11
	v_cvt_pk_f32_fp8_e32 v[10:11], v210
	v_permlane16_swap_b32_e32 v6, v8
	v_permlane16_swap_b32_e32 v7, v9
	v_mul_f32_e32 v10, 0x3d800000, v10
	v_mul_f32_e32 v10, 0xbfb8aa3b, v10
	v_exp_f32_e32 v10, v10
	v_mul_f32_e32 v11, 0x3d800000, v11
	v_mul_f32_e32 v11, 0xbfb8aa3b, v11
	v_exp_f32_e32 v11, v11
	global_store_dwordx4 v[2:3], v[6:9], off offset:128
	ds_read_b128 v[6:9], v5 offset:384
	v_add_f32_e32 v10, 1.0, v10
	v_rcp_f32_e32 v10, v10
	v_add_f32_e32 v11, 1.0, v11
	v_cvt_pk_f32_fp8_sdwa v[12:13], v210 src0_sel:WORD_1
	v_mul_f32_e32 v14, v152, v4
	v_rcp_f32_e32 v11, v11
	s_waitcnt lgkmcnt(0)
	v_mul_f32_e32 v6, v14, v6
	v_mul_f32_e32 v6, v6, v10
	v_mul_f32_e32 v10, v153, v4
	v_mul_f32_e32 v7, v10, v7
	v_mul_f32_e32 v7, v7, v11
	v_mul_f32_e32 v11, 0x3d800000, v12
	v_mul_f32_e32 v12, 0x3d800000, v13
	v_mul_f32_e32 v12, 0xbfb8aa3b, v12
	v_mul_f32_e32 v11, 0xbfb8aa3b, v11
	v_exp_f32_e32 v12, v12
	v_exp_f32_e32 v11, v11
	v_mul_f32_e32 v10, v150, v4
	v_mul_f32_e32 v8, v10, v8
	v_add_f32_e32 v10, 1.0, v12
	v_cvt_pk_f32_fp8_e32 v[12:13], v201
	v_add_f32_e32 v11, 1.0, v11
	v_rcp_f32_e32 v11, v11
	v_rcp_f32_e32 v10, v10
	v_mul_f32_e32 v12, 0x3d800000, v12
	v_mul_f32_e32 v12, 0xbfb8aa3b, v12
	v_mul_f32_e32 v8, v8, v11
	v_mul_f32_e32 v11, v151, v4
	v_exp_f32_e32 v12, v12
	v_mul_f32_e32 v13, 0x3d800000, v13
	v_mul_f32_e32 v9, v11, v9
	v_mul_f32_e32 v13, 0xbfb8aa3b, v13
	v_mul_f32_e32 v9, v9, v10
	v_exp_f32_e32 v13, v13
	v_cvt_pk_bf16_f32 v6, v6, v7
	v_cvt_pk_bf16_f32 v7, v8, v9
	ds_read_b128 v[8:11], v5 offset:448
	v_add_f32_e32 v12, 1.0, v12
	v_rcp_f32_e32 v12, v12
	v_add_f32_e32 v13, 1.0, v13
	v_cvt_pk_f32_fp8_sdwa v[14:15], v201 src0_sel:WORD_1
	v_mul_f32_e32 v16, v148, v4
	v_rcp_f32_e32 v13, v13
	s_waitcnt lgkmcnt(0)
	v_mul_f32_e32 v8, v16, v8
	v_mul_f32_e32 v8, v8, v12
	v_mul_f32_e32 v12, v149, v4
	v_mul_f32_e32 v9, v12, v9
	v_mul_f32_e32 v9, v9, v13
	v_mul_f32_e32 v13, 0x3d800000, v14
	v_mul_f32_e32 v13, 0xbfb8aa3b, v13
	v_exp_f32_e32 v13, v13
	v_mul_f32_e32 v14, 0x3d800000, v15
	v_mul_f32_e32 v14, 0xbfb8aa3b, v14
	v_exp_f32_e32 v14, v14
	v_add_f32_e32 v13, 1.0, v13
	v_mul_f32_e32 v12, v146, v4
	v_rcp_f32_e32 v13, v13
	v_mul_f32_e32 v10, v12, v10
	v_add_f32_e32 v12, 1.0, v14
	v_rcp_f32_e32 v12, v12
	v_mul_f32_e32 v10, v10, v13
	v_mul_f32_e32 v13, v147, v4
	v_mul_f32_e32 v11, v13, v11
	v_mul_f32_e32 v11, v11, v12
	v_cvt_pk_bf16_f32 v8, v8, v9
	v_cvt_pk_bf16_f32 v9, v10, v11
	v_cvt_pk_f32_fp8_e32 v[10:11], v105
	v_permlane16_swap_b32_e32 v6, v8
	v_permlane16_swap_b32_e32 v7, v9
	v_mul_f32_e32 v10, 0x3d800000, v10
	v_mul_f32_e32 v10, 0xbfb8aa3b, v10
	v_exp_f32_e32 v10, v10
	v_mul_f32_e32 v11, 0x3d800000, v11
	v_mul_f32_e32 v11, 0xbfb8aa3b, v11
	v_exp_f32_e32 v11, v11
	global_store_dwordx4 v[2:3], v[6:9], off offset:192
	ds_read_b128 v[6:9], v5 offset:512
	v_add_f32_e32 v10, 1.0, v10
	v_rcp_f32_e32 v10, v10
	v_add_f32_e32 v11, 1.0, v11
	v_cvt_pk_f32_fp8_sdwa v[12:13], v105 src0_sel:WORD_1
	v_mul_f32_e32 v14, v144, v4
	v_rcp_f32_e32 v11, v11
	s_waitcnt lgkmcnt(0)
	v_mul_f32_e32 v6, v14, v6
	v_mul_f32_e32 v6, v6, v10
	v_mul_f32_e32 v10, v145, v4
	v_mul_f32_e32 v7, v10, v7
	v_mul_f32_e32 v7, v7, v11
	v_mul_f32_e32 v11, 0x3d800000, v12
	v_mul_f32_e32 v12, 0x3d800000, v13
	v_mul_f32_e32 v12, 0xbfb8aa3b, v12
	v_mul_f32_e32 v11, 0xbfb8aa3b, v11
	v_exp_f32_e32 v12, v12
	v_exp_f32_e32 v11, v11
	v_mul_f32_e32 v10, v142, v4
	v_mul_f32_e32 v8, v10, v8
	v_add_f32_e32 v10, 1.0, v12
	v_cvt_pk_f32_fp8_e32 v[12:13], v213
	v_add_f32_e32 v11, 1.0, v11
	v_rcp_f32_e32 v11, v11
	v_rcp_f32_e32 v10, v10
	v_mul_f32_e32 v12, 0x3d800000, v12
	v_mul_f32_e32 v12, 0xbfb8aa3b, v12
	v_mul_f32_e32 v8, v8, v11
	v_mul_f32_e32 v11, v143, v4
	v_exp_f32_e32 v12, v12
	v_mul_f32_e32 v13, 0x3d800000, v13
	v_mul_f32_e32 v9, v11, v9
	v_mul_f32_e32 v13, 0xbfb8aa3b, v13
	v_mul_f32_e32 v9, v9, v10
	v_exp_f32_e32 v13, v13
	v_cvt_pk_bf16_f32 v6, v6, v7
	v_cvt_pk_bf16_f32 v7, v8, v9
	ds_read_b128 v[8:11], v5 offset:576
	v_add_f32_e32 v12, 1.0, v12
	v_rcp_f32_e32 v12, v12
	v_add_f32_e32 v13, 1.0, v13
	v_cvt_pk_f32_fp8_sdwa v[14:15], v213 src0_sel:WORD_1
	v_mul_f32_e32 v16, v140, v4
	v_rcp_f32_e32 v13, v13
	s_waitcnt lgkmcnt(0)
	v_mul_f32_e32 v8, v16, v8
	v_mul_f32_e32 v8, v8, v12
	v_mul_f32_e32 v12, v141, v4
	v_mul_f32_e32 v9, v12, v9
	v_mul_f32_e32 v9, v9, v13
	v_mul_f32_e32 v13, 0x3d800000, v14
	v_mul_f32_e32 v13, 0xbfb8aa3b, v13
	v_exp_f32_e32 v13, v13
	v_mul_f32_e32 v14, 0x3d800000, v15
	v_mul_f32_e32 v14, 0xbfb8aa3b, v14
	v_exp_f32_e32 v14, v14
	v_add_f32_e32 v13, 1.0, v13
	v_mul_f32_e32 v12, v138, v4
	v_rcp_f32_e32 v13, v13
	v_mul_f32_e32 v10, v12, v10
	v_add_f32_e32 v12, 1.0, v14
	v_rcp_f32_e32 v12, v12
	v_mul_f32_e32 v10, v10, v13
	v_mul_f32_e32 v13, v139, v4
	v_mul_f32_e32 v11, v13, v11
	v_mul_f32_e32 v11, v11, v12
	v_cvt_pk_bf16_f32 v8, v8, v9
	v_cvt_pk_bf16_f32 v9, v10, v11
	v_cvt_pk_f32_fp8_e32 v[10:11], v214
	v_permlane16_swap_b32_e32 v6, v8
	v_permlane16_swap_b32_e32 v7, v9
	v_mul_f32_e32 v10, 0x3d800000, v10
	v_mul_f32_e32 v10, 0xbfb8aa3b, v10
	v_exp_f32_e32 v10, v10
	v_mul_f32_e32 v11, 0x3d800000, v11
	v_mul_f32_e32 v11, 0xbfb8aa3b, v11
	v_exp_f32_e32 v11, v11
	global_store_dwordx4 v[2:3], v[6:9], off offset:256
	ds_read_b128 v[6:9], v5 offset:640
	v_add_f32_e32 v10, 1.0, v10
	v_rcp_f32_e32 v10, v10
	v_add_f32_e32 v11, 1.0, v11
	v_cvt_pk_f32_fp8_sdwa v[12:13], v214 src0_sel:WORD_1
	v_mul_f32_e32 v14, v136, v4
	v_rcp_f32_e32 v11, v11
	s_waitcnt lgkmcnt(0)
	v_mul_f32_e32 v6, v14, v6
	v_mul_f32_e32 v6, v6, v10
	v_mul_f32_e32 v10, v137, v4
	v_mul_f32_e32 v7, v10, v7
	v_mul_f32_e32 v7, v7, v11
	v_mul_f32_e32 v11, 0x3d800000, v12
	v_mul_f32_e32 v12, 0x3d800000, v13
	v_mul_f32_e32 v12, 0xbfb8aa3b, v12
	v_mul_f32_e32 v11, 0xbfb8aa3b, v11
	v_exp_f32_e32 v12, v12
	v_exp_f32_e32 v11, v11
	v_mul_f32_e32 v10, v134, v4
	v_mul_f32_e32 v8, v10, v8
	v_add_f32_e32 v10, 1.0, v12
	v_cvt_pk_f32_fp8_e32 v[12:13], v215
	v_add_f32_e32 v11, 1.0, v11
	v_rcp_f32_e32 v11, v11
	v_rcp_f32_e32 v10, v10
	v_mul_f32_e32 v12, 0x3d800000, v12
	v_mul_f32_e32 v12, 0xbfb8aa3b, v12
	v_mul_f32_e32 v8, v8, v11
	v_mul_f32_e32 v11, v135, v4
	v_exp_f32_e32 v12, v12
	v_mul_f32_e32 v13, 0x3d800000, v13
	v_mul_f32_e32 v9, v11, v9
	v_mul_f32_e32 v13, 0xbfb8aa3b, v13
	v_mul_f32_e32 v9, v9, v10
	v_exp_f32_e32 v13, v13
	v_cvt_pk_bf16_f32 v6, v6, v7
	v_cvt_pk_bf16_f32 v7, v8, v9
	ds_read_b128 v[8:11], v5 offset:704
	v_add_f32_e32 v12, 1.0, v12
	v_rcp_f32_e32 v12, v12
	v_add_f32_e32 v13, 1.0, v13
	v_cvt_pk_f32_fp8_sdwa v[14:15], v215 src0_sel:WORD_1
	v_mul_f32_e32 v16, v132, v4
	v_rcp_f32_e32 v13, v13
	s_waitcnt lgkmcnt(0)
	v_mul_f32_e32 v8, v16, v8
	v_mul_f32_e32 v8, v8, v12
	v_mul_f32_e32 v12, v133, v4
	v_mul_f32_e32 v9, v12, v9
	v_mul_f32_e32 v9, v9, v13
	v_mul_f32_e32 v13, 0x3d800000, v14
	v_mul_f32_e32 v13, 0xbfb8aa3b, v13
	v_exp_f32_e32 v13, v13
	v_mul_f32_e32 v14, 0x3d800000, v15
	v_mul_f32_e32 v14, 0xbfb8aa3b, v14
	v_exp_f32_e32 v14, v14
	v_add_f32_e32 v13, 1.0, v13
	v_mul_f32_e32 v12, v130, v4
	v_rcp_f32_e32 v13, v13
	v_mul_f32_e32 v10, v12, v10
	v_add_f32_e32 v12, 1.0, v14
	v_rcp_f32_e32 v12, v12
	v_mul_f32_e32 v10, v10, v13
	v_mul_f32_e32 v13, v131, v4
	v_mul_f32_e32 v11, v13, v11
	v_mul_f32_e32 v11, v11, v12
	v_cvt_pk_bf16_f32 v8, v8, v9
	v_cvt_pk_bf16_f32 v9, v10, v11
	v_cvt_pk_f32_fp8_e32 v[10:11], v202
	v_permlane16_swap_b32_e32 v6, v8
	v_permlane16_swap_b32_e32 v7, v9
	v_mul_f32_e32 v10, 0x3d800000, v10
	v_mul_f32_e32 v10, 0xbfb8aa3b, v10
	v_exp_f32_e32 v10, v10
	v_mul_f32_e32 v11, 0x3d800000, v11
	v_mul_f32_e32 v11, 0xbfb8aa3b, v11
	v_exp_f32_e32 v11, v11
	global_store_dwordx4 v[2:3], v[6:9], off offset:320
	ds_read_b128 v[6:9], v5 offset:768
	v_add_f32_e32 v10, 1.0, v10
	v_rcp_f32_e32 v10, v10
	v_add_f32_e32 v11, 1.0, v11
	v_cvt_pk_f32_fp8_sdwa v[12:13], v202 src0_sel:WORD_1
	v_mul_f32_e32 v14, v128, v4
	v_rcp_f32_e32 v11, v11
	s_waitcnt lgkmcnt(0)
	v_mul_f32_e32 v6, v14, v6
	v_mul_f32_e32 v6, v6, v10
	v_mul_f32_e32 v10, v129, v4
	v_mul_f32_e32 v7, v10, v7
	v_mul_f32_e32 v7, v7, v11
	v_mul_f32_e32 v11, 0x3d800000, v12
	v_mul_f32_e32 v12, 0x3d800000, v13
	v_mul_f32_e32 v12, 0xbfb8aa3b, v12
	v_mul_f32_e32 v11, 0xbfb8aa3b, v11
	v_exp_f32_e32 v12, v12
	v_exp_f32_e32 v11, v11
	v_mul_f32_e32 v10, v126, v4
	v_mul_f32_e32 v8, v10, v8
	v_add_f32_e32 v10, 1.0, v12
	v_cvt_pk_f32_fp8_e32 v[12:13], v203
	v_add_f32_e32 v11, 1.0, v11
	v_rcp_f32_e32 v11, v11
	v_rcp_f32_e32 v10, v10
	v_mul_f32_e32 v12, 0x3d800000, v12
	v_mul_f32_e32 v12, 0xbfb8aa3b, v12
	v_mul_f32_e32 v8, v8, v11
	v_mul_f32_e32 v11, v127, v4
	v_exp_f32_e32 v12, v12
	v_mul_f32_e32 v13, 0x3d800000, v13
	v_mul_f32_e32 v9, v11, v9
	v_mul_f32_e32 v13, 0xbfb8aa3b, v13
	v_mul_f32_e32 v9, v9, v10
	v_exp_f32_e32 v13, v13
	v_cvt_pk_bf16_f32 v6, v6, v7
	v_cvt_pk_bf16_f32 v7, v8, v9
	ds_read_b128 v[8:11], v5 offset:832
	v_add_f32_e32 v12, 1.0, v12
	v_rcp_f32_e32 v12, v12
	v_add_f32_e32 v13, 1.0, v13
	v_cvt_pk_f32_fp8_sdwa v[14:15], v203 src0_sel:WORD_1
	v_mul_f32_e32 v16, v124, v4
	v_rcp_f32_e32 v13, v13
	s_waitcnt lgkmcnt(0)
	v_mul_f32_e32 v8, v16, v8
	v_mul_f32_e32 v8, v8, v12
	v_mul_f32_e32 v12, v125, v4
	v_mul_f32_e32 v9, v12, v9
	v_mul_f32_e32 v9, v9, v13
	v_mul_f32_e32 v13, 0x3d800000, v14
	v_mul_f32_e32 v13, 0xbfb8aa3b, v13
	v_exp_f32_e32 v13, v13
	v_mul_f32_e32 v14, 0x3d800000, v15
	v_mul_f32_e32 v14, 0xbfb8aa3b, v14
	v_exp_f32_e32 v14, v14
	v_add_f32_e32 v13, 1.0, v13
	v_mul_f32_e32 v12, v122, v4
	v_rcp_f32_e32 v13, v13
	v_mul_f32_e32 v10, v12, v10
	v_add_f32_e32 v12, 1.0, v14
	v_rcp_f32_e32 v12, v12
	v_mul_f32_e32 v10, v10, v13
	v_mul_f32_e32 v13, v123, v4
	v_mul_f32_e32 v11, v13, v11
	v_mul_f32_e32 v11, v11, v12
	v_cvt_pk_bf16_f32 v8, v8, v9
	v_cvt_pk_bf16_f32 v9, v10, v11
	v_cvt_pk_f32_fp8_e32 v[10:11], v216
	v_permlane16_swap_b32_e32 v6, v8
	v_permlane16_swap_b32_e32 v7, v9
	v_mul_f32_e32 v10, 0x3d800000, v10
	v_mul_f32_e32 v10, 0xbfb8aa3b, v10
	v_exp_f32_e32 v10, v10
	v_mul_f32_e32 v11, 0x3d800000, v11
	v_mul_f32_e32 v11, 0xbfb8aa3b, v11
	v_exp_f32_e32 v11, v11
	global_store_dwordx4 v[2:3], v[6:9], off offset:384
	ds_read_b128 v[6:9], v5 offset:896
	v_add_f32_e32 v10, 1.0, v10
	v_rcp_f32_e32 v10, v10
	v_add_f32_e32 v11, 1.0, v11
	v_cvt_pk_f32_fp8_sdwa v[12:13], v216 src0_sel:WORD_1
	v_mul_f32_e32 v14, v120, v4
	v_rcp_f32_e32 v11, v11
	s_waitcnt lgkmcnt(0)
	v_mul_f32_e32 v6, v14, v6
	v_mul_f32_e32 v6, v6, v10
	v_mul_f32_e32 v10, v121, v4
	v_mul_f32_e32 v7, v10, v7
	v_mul_f32_e32 v7, v7, v11
	v_mul_f32_e32 v11, 0x3d800000, v12
	v_mul_f32_e32 v12, 0x3d800000, v13
	v_mul_f32_e32 v12, 0xbfb8aa3b, v12
	v_mul_f32_e32 v11, 0xbfb8aa3b, v11
	v_exp_f32_e32 v12, v12
	v_exp_f32_e32 v11, v11
	v_mul_f32_e32 v10, v118, v4
	v_mul_f32_e32 v8, v10, v8
	v_add_f32_e32 v10, 1.0, v12
	v_cvt_pk_f32_fp8_e32 v[12:13], v217
	v_add_f32_e32 v11, 1.0, v11
	v_rcp_f32_e32 v11, v11
	v_rcp_f32_e32 v10, v10
	v_mul_f32_e32 v12, 0x3d800000, v12
	v_mul_f32_e32 v12, 0xbfb8aa3b, v12
	v_mul_f32_e32 v8, v8, v11
	v_mul_f32_e32 v11, v119, v4
	v_exp_f32_e32 v12, v12
	v_mul_f32_e32 v9, v11, v9
	v_mul_f32_e32 v9, v9, v10
	v_cvt_pk_bf16_f32 v6, v6, v7
	v_cvt_pk_bf16_f32 v7, v8, v9
	ds_read_b128 v[8:11], v5 offset:960
	v_add_f32_e32 v12, 1.0, v12
	v_mul_f32_e32 v13, 0x3d800000, v13
	v_rcp_f32_e32 v12, v12
	v_cvt_pk_f32_fp8_sdwa v[14:15], v217 src0_sel:WORD_1
	v_mul_f32_e32 v13, 0xbfb8aa3b, v13
	v_mul_f32_e32 v5, v116, v4
	v_exp_f32_e32 v13, v13
	s_waitcnt lgkmcnt(0)
	v_mul_f32_e32 v5, v5, v8
	v_mul_f32_e32 v5, v5, v12
	v_mul_f32_e32 v12, v117, v4
	v_mul_f32_e32 v9, v12, v9
	v_mul_f32_e32 v12, 0x3d800000, v14
	v_add_f32_e32 v8, 1.0, v13
	v_mul_f32_e32 v12, 0xbfb8aa3b, v12
	v_mul_f32_e32 v13, 0x3d800000, v15
	v_rcp_f32_e32 v8, v8
	v_exp_f32_e32 v12, v12
	v_mul_f32_e32 v13, 0xbfb8aa3b, v13
	v_exp_f32_e32 v13, v13
	v_mul_f32_e32 v8, v9, v8
	v_mul_f32_e32 v9, v114, v4
	v_add_f32_e32 v12, 1.0, v12
	v_rcp_f32_e32 v12, v12
	v_mul_f32_e32 v9, v9, v10
	v_add_f32_e32 v10, 1.0, v13
	v_rcp_f32_e32 v10, v10
	v_mul_f32_e32 v4, v115, v4
	v_mul_f32_e32 v9, v9, v12
	v_mul_f32_e32 v4, v4, v11
	v_mul_f32_e32 v4, v4, v10
	v_cvt_pk_bf16_f32 v8, v5, v8
	v_cvt_pk_bf16_f32 v9, v9, v4
	s_nop 0
	v_permlane16_swap_b32_e32 v6, v8
	v_permlane16_swap_b32_e32 v7, v9
	global_store_dwordx4 v[2:3], v[6:9], off offset:448
	s_barrier
	s_cbranch_scc1 .LBB0_778

.LBB0_776:
	s_or_b32 s48, s34, s30
	s_ashr_i32 s49, s48, 31
	s_lshl_b64 s[48:49], s[48:49], 4
	s_and_b64 s[84:85], s[44:45], exec
	s_cselect_b32 s18, s80, s31
	s_or_b32 s18, s48, s18
	s_mul_i32 s19, s18, 0x11000
	s_mul_hi_u32 s18, s18, 0x11000
	s_mul_i32 s35, s49, 0x11000
	s_add_i32 s18, s18, s35
	s_add_u32 s48, s53, s19
	s_addc_u32 s49, s54, s18
	s_lshl_b32 s18, s34, 11
	s_add_i32 s18, s18, 0
	s_add_i32 s18, s18, 0x18000
	v_mov_b32_e32 v52, v230
	v_mov_b32_e32 v18, s18
	v_lshl_add_u64 v[54:55], s[48:49], 0, v[86:87]
	v_mov_b32_e32 v107, v87
	ds_read_b32 v51, v18 offset:1536
	v_lshl_add_u64 v[18:19], v[54:55], 0, v[106:107]
	v_mov_b32_e32 v109, v87
	v_lshl_add_u64 v[20:21], v[54:55], 0, v[108:109]
	global_load_dwordx4 v[46:49], v[18:19], off
	global_load_dwordx4 v[42:45], v[20:21], off
	v_add_co_u32_e32 v18, vcc, s72, v18
	v_ashrrev_i32_e32 v53, 4, v52
	s_nop 0
	v_addc_co_u32_e32 v19, vcc, 0, v19, vcc
	v_add_co_u32_e32 v20, vcc, s72, v20
	v_and_b32_e32 v56, 15, v52
	s_nop 0
	v_addc_co_u32_e32 v21, vcc, 0, v21, vcc
	global_load_dwordx4 v[34:37], v[18:19], off
	global_load_dwordx4 v[38:41], v[20:21], off
	v_lshlrev_b32_e32 v18, 2, v52
	v_and_b32_e32 v30, 12, v18
	v_bfe_u32 v31, v52, 2, 2
	v_lshlrev_b32_e32 v61, 8, v56
	v_bitop3_b32 v18, v30, v53, v31 bitop3:0x36
	v_add_u32_e32 v50, s62, v61
	v_lshlrev_b32_e32 v58, 4, v18
	v_add_u32_e32 v33, v50, v58
	ds_read_b128 v[18:21], v33
	v_add_u32_e32 v22, 4, v53
	v_bitop3_b32 v22, v30, v22, v31 bitop3:0x36
	v_lshlrev_b32_e32 v60, 4, v22
	v_add_u32_e32 v64, v50, v60
	ds_read_b128 v[22:25], v64
	v_add_u32_e32 v26, 8, v53
	v_bitop3_b32 v26, v30, v26, v31 bitop3:0x36
	v_lshlrev_b32_e32 v59, 4, v26
	v_or_b32_e32 v32, s66, v56
	v_add_u32_e32 v63, v50, v59
	v_lshl_add_u32 v62, v32, 2, s18
	ds_read_b128 v[26:29], v63
	ds_read_b32 v67, v62 offset:1024
	s_waitcnt vmcnt(7) lgkmcnt(3)
	v_mfma_f32_16x16x32_bf16 v[18:21], v[18:21], v[2:5], 0
	v_add_u32_e32 v57, 12, v53
	v_bitop3_b32 v30, v30, v57, v31 bitop3:0x36
	v_lshlrev_b32_e32 v57, 4, v30
	v_and_b32_e32 v66, -16, v52
	v_add_u32_e32 v65, v50, v57
	ds_read_b128 v[68:71], v65
	s_waitcnt vmcnt(6) lgkmcnt(3)
	v_mfma_f32_16x16x32_bf16 v[18:21], v[22:25], v[6:9], v[18:21]
	v_add_u32_e32 v66, s18, v66
	ds_read_b128 v[22:25], v66 offset:512
	s_waitcnt lgkmcnt(2)
	v_max_f32_e32 v30, v67, v67
	s_waitcnt vmcnt(5)
	v_mfma_f32_16x16x32_bf16 v[18:21], v[26:29], v[10:13], v[18:21]
	v_max_f32_e32 v26, v51, v51
	v_max_f32_e32 v82, v26, v30
	s_waitcnt lgkmcnt(0)
	v_sub_f32_e32 v22, v22, v82
	v_lshlrev_b32_e32 v50, 2, v53
	v_min_f32_e32 v22, 0, v22
	v_cmp_le_i32_e32 vcc, v50, v32
	v_mul_f32_e32 v22, 0x3fb8aa3b, v22
	s_waitcnt vmcnt(4)
	v_mfma_f32_16x16x32_bf16 v[18:21], v[68:71], v[14:17], v[18:21]
	v_cndmask_b32_e64 v26, 0, 1, vcc
	v_exp_f32_e32 v22, v22
	v_cmp_ge_i32_e32 vcc, v50, v32
	v_sub_f32_e32 v23, v23, v82
	v_min_f32_e32 v23, 0, v23
	v_cndmask_b32_e64 v27, 0, 1, vcc
	v_cndmask_b32_e64 v26, v27, v26, s[44:45]
	v_and_b32_e32 v26, 1, v26
	v_mul_f32_e32 v18, v18, v22
	v_cmp_eq_u32_e32 vcc, 1, v26
	v_or_b32_e32 v22, 1, v50
	v_mul_f32_e32 v23, 0x3fb8aa3b, v23
	v_cndmask_b32_e32 v18, 0, v18, vcc
	v_cmp_lt_i32_e32 vcc, v50, v32
	v_exp_f32_e32 v23, v23
	v_sub_f32_e32 v24, v24, v82
	v_cndmask_b32_e64 v26, 0, 1, vcc
	v_cmp_ge_i32_e32 vcc, v22, v32
	v_min_f32_e32 v24, 0, v24
	v_mul_f32_e32 v19, v19, v23
	v_cndmask_b32_e64 v22, 0, 1, vcc
	v_cndmask_b32_e64 v22, v22, v26, s[44:45]
	v_and_b32_e32 v22, 1, v22
	v_cmp_eq_u32_e32 vcc, 1, v22
	v_or_b32_e32 v22, 2, v50
	v_mul_f32_e32 v24, 0x3fb8aa3b, v24
	v_cndmask_b32_e32 v19, 0, v19, vcc
	v_cmp_le_i32_e32 vcc, v22, v32
	v_exp_f32_e32 v24, v24
	v_cvt_pk_bf16_f32 v18, v18, v19
	v_sub_f32_e32 v51, v51, v82
	v_cndmask_b32_e64 v23, 0, 1, vcc
	v_cmp_ge_i32_e32 vcc, v22, v32
	v_mul_f32_e32 v20, v20, v24
	v_sub_f32_e32 v24, v25, v82
	v_cndmask_b32_e64 v22, 0, 1, vcc
	v_cndmask_b32_e64 v22, v22, v23, s[44:45]
	v_and_b32_e32 v22, 1, v22
	v_cmp_eq_u32_e32 vcc, 1, v22
	v_or_b32_e32 v22, 3, v50
	v_min_f32_e32 v24, 0, v24
	v_cndmask_b32_e32 v20, 0, v20, vcc
	v_cmp_le_i32_e32 vcc, v22, v32
	v_mul_f32_e32 v24, 0x3fb8aa3b, v24
	v_exp_f32_e32 v24, v24
	v_cndmask_b32_e64 v23, 0, 1, vcc
	v_cmp_ge_i32_e32 vcc, v22, v32
	v_mul_f32_e32 v51, 0x3fb8aa3b, v51
	v_mul_f32_e32 v21, v21, v24
	v_cndmask_b32_e64 v22, 0, 1, vcc
	v_cndmask_b32_e64 v22, v22, v23, s[44:45]
	v_and_b32_e32 v22, 1, v22
	v_cmp_eq_u32_e32 vcc, 1, v22
	v_exp_f32_e32 v180, v51
	v_and_or_b32 v51, v187, 64, v56
	v_cndmask_b32_e32 v21, 0, v21, vcc
	v_cvt_pk_bf16_f32 v19, v20, v21
	ds_read_b128 v[20:23], v33 offset:4096
	ds_read_b128 v[24:27], v64 offset:4096
	ds_read_b128 v[28:31], v66 offset:576
	s_waitcnt lgkmcnt(2)
	v_mfma_f32_16x16x32_bf16 v[20:23], v[20:23], v[2:5], 0
	ds_read_b128 v[68:71], v63 offset:4096
	v_lshlrev_b32_e32 v51, 2, v51
	s_waitcnt lgkmcnt(2)
	v_mfma_f32_16x16x32_bf16 v[20:23], v[24:27], v[6:9], v[20:23]
	ds_read_b128 v[24:27], v65 offset:4096
	s_waitcnt lgkmcnt(1)
	v_mfma_f32_16x16x32_bf16 v[20:23], v[68:71], v[10:13], v[20:23]
	s_waitcnt lgkmcnt(0)
	v_mfma_f32_16x16x32_bf16 v[20:23], v[24:27], v[14:17], v[20:23]
	v_sub_f32_e32 v26, v28, v82
	v_min_f32_e32 v26, 0, v26
	v_mul_f32_e32 v26, 0x3fb8aa3b, v26
	v_exp_f32_e32 v26, v26
	v_add_u32_e32 v24, 16, v50
	v_cmp_le_i32_e32 vcc, v24, v32
	s_nop 1
	v_mul_f32_e32 v20, v20, v26
	v_cndmask_b32_e64 v25, 0, 1, vcc
	v_cmp_ge_i32_e32 vcc, v24, v32
	v_sub_f32_e32 v26, v29, v82
	v_min_f32_e32 v26, 0, v26
	v_cndmask_b32_e64 v24, 0, 1, vcc
	v_cndmask_b32_e64 v24, v24, v25, s[44:45]
	v_and_b32_e32 v24, 1, v24
	v_mul_f32_e32 v26, 0x3fb8aa3b, v26
	v_cmp_eq_u32_e32 vcc, 1, v24
	v_add_u32_e32 v24, 17, v50
	v_exp_f32_e32 v26, v26
	v_cndmask_b32_e32 v20, 0, v20, vcc
	v_cmp_le_i32_e32 vcc, v24, v32
	v_mul_f32_e32 v21, v21, v26
	s_nop 0
	v_cndmask_b32_e64 v25, 0, 1, vcc
	v_cmp_ge_i32_e32 vcc, v24, v32
	v_sub_f32_e32 v26, v30, v82
	v_min_f32_e32 v26, 0, v26
	v_cndmask_b32_e64 v24, 0, 1, vcc
	v_cndmask_b32_e64 v24, v24, v25, s[44:45]
	v_and_b32_e32 v24, 1, v24
	v_cmp_eq_u32_e32 vcc, 1, v24
	v_add_u32_e32 v24, 18, v50
	v_mul_f32_e32 v26, 0x3fb8aa3b, v26
	v_cndmask_b32_e32 v21, 0, v21, vcc
	v_cmp_le_i32_e32 vcc, v24, v32
	v_exp_f32_e32 v26, v26
	v_cvt_pk_bf16_f32 v20, v20, v21
	s_nop 0
	v_cndmask_b32_e64 v25, 0, 1, vcc
	v_cmp_ge_i32_e32 vcc, v24, v32
	v_mul_f32_e32 v22, v22, v26
	v_sub_f32_e32 v26, v31, v82
	v_cndmask_b32_e64 v24, 0, 1, vcc
	v_cndmask_b32_e64 v24, v24, v25, s[44:45]
	v_and_b32_e32 v24, 1, v24
	v_cmp_eq_u32_e32 vcc, 1, v24
	v_add_u32_e32 v24, 19, v50
	v_min_f32_e32 v26, 0, v26
	v_cndmask_b32_e32 v22, 0, v22, vcc
	v_cmp_le_i32_e32 vcc, v24, v32
	v_mul_f32_e32 v26, 0x3fb8aa3b, v26
	v_exp_f32_e32 v26, v26
	v_cndmask_b32_e64 v25, 0, 1, vcc
	v_cmp_ge_i32_e32 vcc, v24, v32
	v_mul_f32_e32 v23, v23, v26
	s_nop 0
	v_cndmask_b32_e64 v24, 0, 1, vcc
	v_cndmask_b32_e64 v24, v24, v25, s[44:45]
	v_and_b32_e32 v24, 1, v24
	v_cmp_eq_u32_e32 vcc, 1, v24
	s_nop 1
	v_cndmask_b32_e32 v23, 0, v23, vcc
	v_cvt_pk_bf16_f32 v21, v22, v23
	ds_read_b128 v[22:25], v33 offset:8192
	ds_read_b128 v[26:29], v64 offset:8192
	ds_read_b128 v[68:71], v66 offset:640
	s_waitcnt lgkmcnt(2)
	v_mfma_f32_16x16x32_bf16 v[22:25], v[22:25], v[2:5], 0
	ds_read_b128 v[72:75], v63 offset:8192
	s_waitcnt lgkmcnt(2)
	v_mfma_f32_16x16x32_bf16 v[22:25], v[26:29], v[6:9], v[22:25]
	ds_read_b128 v[26:29], v65 offset:8192
	s_waitcnt lgkmcnt(1)
	v_mfma_f32_16x16x32_bf16 v[22:25], v[72:75], v[10:13], v[22:25]
	s_waitcnt lgkmcnt(0)
	v_mfma_f32_16x16x32_bf16 v[22:25], v[26:29], v[14:17], v[22:25]
	v_sub_f32_e32 v28, v68, v82
	v_min_f32_e32 v28, 0, v28
	v_mul_f32_e32 v28, 0x3fb8aa3b, v28
	v_exp_f32_e32 v28, v28
	v_add_u32_e32 v26, 32, v50
	v_cmp_le_i32_e32 vcc, v26, v32
	s_nop 1
	v_mul_f32_e32 v22, v22, v28
	v_cndmask_b32_e64 v27, 0, 1, vcc
	v_cmp_ge_i32_e32 vcc, v26, v32
	v_sub_f32_e32 v28, v69, v82
	v_min_f32_e32 v28, 0, v28
	v_cndmask_b32_e64 v26, 0, 1, vcc
	v_cndmask_b32_e64 v26, v26, v27, s[44:45]
	v_and_b32_e32 v26, 1, v26
	v_mul_f32_e32 v28, 0x3fb8aa3b, v28
	v_cmp_eq_u32_e32 vcc, 1, v26
	v_add_u32_e32 v26, 33, v50
	v_exp_f32_e32 v28, v28
	v_cndmask_b32_e32 v22, 0, v22, vcc
	v_cmp_le_i32_e32 vcc, v26, v32
	v_mul_f32_e32 v23, v23, v28
	s_nop 0
	v_cndmask_b32_e64 v27, 0, 1, vcc
	v_cmp_ge_i32_e32 vcc, v26, v32
	v_sub_f32_e32 v28, v70, v82
	v_min_f32_e32 v28, 0, v28
	v_cndmask_b32_e64 v26, 0, 1, vcc
	v_cndmask_b32_e64 v26, v26, v27, s[44:45]
	v_and_b32_e32 v26, 1, v26
	v_cmp_eq_u32_e32 vcc, 1, v26
	v_add_u32_e32 v26, 34, v50
	v_mul_f32_e32 v28, 0x3fb8aa3b, v28
	v_cndmask_b32_e32 v23, 0, v23, vcc
	v_cmp_le_i32_e32 vcc, v26, v32
	v_exp_f32_e32 v28, v28
	v_cvt_pk_bf16_f32 v22, v22, v23
	s_nop 0
	v_cndmask_b32_e64 v27, 0, 1, vcc
	v_cmp_ge_i32_e32 vcc, v26, v32
	v_mul_f32_e32 v24, v24, v28
	v_sub_f32_e32 v28, v71, v82
	v_cndmask_b32_e64 v26, 0, 1, vcc
	v_cndmask_b32_e64 v26, v26, v27, s[44:45]
	v_and_b32_e32 v26, 1, v26
	v_cmp_eq_u32_e32 vcc, 1, v26
	v_add_u32_e32 v26, 35, v50
	v_min_f32_e32 v28, 0, v28
	v_cndmask_b32_e32 v24, 0, v24, vcc
	v_cmp_le_i32_e32 vcc, v26, v32
	v_mul_f32_e32 v28, 0x3fb8aa3b, v28
	v_exp_f32_e32 v28, v28
	v_cndmask_b32_e64 v27, 0, 1, vcc
	v_cmp_ge_i32_e32 vcc, v26, v32
	v_mul_f32_e32 v25, v25, v28
	s_nop 0
	v_cndmask_b32_e64 v26, 0, 1, vcc
	v_cndmask_b32_e64 v26, v26, v27, s[44:45]
	v_and_b32_e32 v26, 1, v26
	v_cmp_eq_u32_e32 vcc, 1, v26
	s_nop 1
	v_cndmask_b32_e32 v25, 0, v25, vcc
	v_cvt_pk_bf16_f32 v23, v24, v25
	ds_read_b128 v[24:27], v33 offset:12288
	ds_read_b128 v[28:31], v64 offset:12288
	ds_read_b128 v[68:71], v66 offset:704
	s_waitcnt lgkmcnt(2)
	v_mfma_f32_16x16x32_bf16 v[24:27], v[24:27], v[2:5], 0
	ds_read_b128 v[72:75], v63 offset:12288
	s_waitcnt lgkmcnt(2)
	v_mfma_f32_16x16x32_bf16 v[24:27], v[28:31], v[6:9], v[24:27]
	ds_read_b128 v[28:31], v65 offset:12288
	s_waitcnt lgkmcnt(1)
	v_mfma_f32_16x16x32_bf16 v[24:27], v[72:75], v[10:13], v[24:27]
	s_waitcnt lgkmcnt(0)
	v_mfma_f32_16x16x32_bf16 v[24:27], v[28:31], v[14:17], v[24:27]
	v_sub_f32_e32 v30, v68, v82
	v_min_f32_e32 v30, 0, v30
	v_mul_f32_e32 v30, 0x3fb8aa3b, v30
	v_exp_f32_e32 v30, v30
	v_add_u32_e32 v28, 48, v50
	v_cmp_le_i32_e32 vcc, v28, v32
	s_nop 1
	v_mul_f32_e32 v24, v24, v30
	v_cndmask_b32_e64 v29, 0, 1, vcc
	v_cmp_ge_i32_e32 vcc, v28, v32
	v_sub_f32_e32 v30, v69, v82
	v_min_f32_e32 v30, 0, v30
	v_cndmask_b32_e64 v28, 0, 1, vcc
	v_cndmask_b32_e64 v28, v28, v29, s[44:45]
	v_and_b32_e32 v28, 1, v28
	v_mul_f32_e32 v30, 0x3fb8aa3b, v30
	v_cmp_eq_u32_e32 vcc, 1, v28
	v_add_u32_e32 v28, 49, v50
	v_exp_f32_e32 v30, v30
	v_cndmask_b32_e32 v24, 0, v24, vcc
	v_cmp_le_i32_e32 vcc, v28, v32
	v_mul_f32_e32 v25, v25, v30
	s_nop 0
	v_cndmask_b32_e64 v29, 0, 1, vcc
	v_cmp_ge_i32_e32 vcc, v28, v32
	v_sub_f32_e32 v30, v70, v82
	v_min_f32_e32 v30, 0, v30
	v_cndmask_b32_e64 v28, 0, 1, vcc
	v_cndmask_b32_e64 v28, v28, v29, s[44:45]
	v_and_b32_e32 v28, 1, v28
	v_cmp_eq_u32_e32 vcc, 1, v28
	v_add_u32_e32 v28, 50, v50
	v_mul_f32_e32 v30, 0x3fb8aa3b, v30
	v_cndmask_b32_e32 v25, 0, v25, vcc
	v_cmp_le_i32_e32 vcc, v28, v32
	v_exp_f32_e32 v30, v30
	v_cvt_pk_bf16_f32 v24, v24, v25
	s_nop 0
	v_cndmask_b32_e64 v29, 0, 1, vcc
	v_cmp_ge_i32_e32 vcc, v28, v32
	v_mul_f32_e32 v26, v26, v30
	v_sub_f32_e32 v30, v71, v82
	v_cndmask_b32_e64 v28, 0, 1, vcc
	v_cndmask_b32_e64 v28, v28, v29, s[44:45]
	v_and_b32_e32 v28, 1, v28
	v_cmp_eq_u32_e32 vcc, 1, v28
	v_add_u32_e32 v28, 51, v50
	v_min_f32_e32 v30, 0, v30
	v_cndmask_b32_e32 v26, 0, v26, vcc
	v_cmp_le_i32_e32 vcc, v28, v32
	v_mul_f32_e32 v30, 0x3fb8aa3b, v30
	v_exp_f32_e32 v30, v30
	v_cndmask_b32_e64 v29, 0, 1, vcc
	v_cmp_ge_i32_e32 vcc, v28, v32
	v_mul_f32_e32 v27, v27, v30
	s_nop 0
	v_cndmask_b32_e64 v28, 0, 1, vcc
	v_cndmask_b32_e64 v28, v28, v29, s[44:45]
	v_and_b32_e32 v28, 1, v28
	v_cmp_eq_u32_e32 vcc, 1, v28
	v_add_u32_e32 v30, 64, v50
	s_nop 0
	v_cndmask_b32_e32 v27, 0, v27, vcc
	v_cvt_pk_bf16_f32 v25, v26, v27
	ds_read_b128 v[26:29], v33 offset:16384
	ds_read_b128 v[68:71], v64 offset:16384
	ds_read_b128 v[72:75], v66 offset:768
	s_waitcnt lgkmcnt(2)
	v_mfma_f32_16x16x32_bf16 v[26:29], v[26:29], v[2:5], 0
	ds_read_b128 v[76:79], v63 offset:16384
	s_waitcnt lgkmcnt(1)
	v_sub_f32_e32 v67, v72, v82
	v_min_f32_e32 v67, 0, v67
	v_mfma_f32_16x16x32_bf16 v[26:29], v[68:71], v[6:9], v[26:29]
	ds_read_b128 v[68:71], v65 offset:16384
	v_mul_f32_e32 v67, 0x3fb8aa3b, v67
	v_exp_f32_e32 v67, v67
	s_waitcnt lgkmcnt(1)
	v_mfma_f32_16x16x32_bf16 v[26:29], v[76:79], v[10:13], v[26:29]
	v_cmp_le_i32_e32 vcc, v30, v32
	s_waitcnt lgkmcnt(0)
	v_mfma_f32_16x16x32_bf16 v[26:29], v[68:71], v[14:17], v[26:29]
	v_cndmask_b32_e64 v31, 0, 1, vcc
	v_cmp_ge_i32_e32 vcc, v30, v32
	s_nop 1
	v_cndmask_b32_e64 v30, 0, 1, vcc
	s_nop 2
	v_mul_f32_e32 v26, v26, v67
	v_sub_f32_e32 v67, v73, v82
	v_cndmask_b32_e64 v30, v30, v31, s[44:45]
	v_min_f32_e32 v67, 0, v67
	v_and_b32_e32 v30, 1, v30
	v_mul_f32_e32 v67, 0x3fb8aa3b, v67
	v_cmp_eq_u32_e32 vcc, 1, v30
	v_add_u32_e32 v30, 0x41, v50
	v_exp_f32_e32 v67, v67
	v_cndmask_b32_e32 v26, 0, v26, vcc
	v_cmp_le_i32_e32 vcc, v30, v32
	v_mul_f32_e32 v27, v27, v67
	s_nop 0
	v_cndmask_b32_e64 v31, 0, 1, vcc
	v_cmp_ge_i32_e32 vcc, v30, v32
	v_sub_f32_e32 v67, v74, v82
	v_min_f32_e32 v67, 0, v67
	v_cndmask_b32_e64 v30, 0, 1, vcc
	v_cndmask_b32_e64 v30, v30, v31, s[44:45]
	v_and_b32_e32 v30, 1, v30
	v_cmp_eq_u32_e32 vcc, 1, v30
	v_add_u32_e32 v30, 0x42, v50
	v_mul_f32_e32 v67, 0x3fb8aa3b, v67
	v_cndmask_b32_e32 v27, 0, v27, vcc
	v_cmp_le_i32_e32 vcc, v30, v32
	v_exp_f32_e32 v67, v67
	v_cvt_pk_bf16_f32 v26, v26, v27
	s_nop 0
	v_cndmask_b32_e64 v31, 0, 1, vcc
	v_cmp_ge_i32_e32 vcc, v30, v32
	v_mul_f32_e32 v28, v28, v67
	v_sub_f32_e32 v67, v75, v82
	v_cndmask_b32_e64 v30, 0, 1, vcc
	v_cndmask_b32_e64 v30, v30, v31, s[44:45]
	v_and_b32_e32 v30, 1, v30
	v_cmp_eq_u32_e32 vcc, 1, v30
	v_add_u32_e32 v30, 0x43, v50
	v_min_f32_e32 v67, 0, v67
	v_cndmask_b32_e32 v28, 0, v28, vcc
	v_cmp_le_i32_e32 vcc, v30, v32
	v_mul_f32_e32 v67, 0x3fb8aa3b, v67
	v_exp_f32_e32 v67, v67
	v_cndmask_b32_e64 v31, 0, 1, vcc
	v_cmp_ge_i32_e32 vcc, v30, v32
	v_mul_f32_e32 v29, v29, v67
	s_nop 0
	v_cndmask_b32_e64 v30, 0, 1, vcc
	v_cndmask_b32_e64 v30, v30, v31, s[44:45]
	v_and_b32_e32 v30, 1, v30
	v_cmp_eq_u32_e32 vcc, 1, v30
	v_add_u32_e32 v67, 0x50, v50
	s_nop 0
	v_cndmask_b32_e32 v29, 0, v29, vcc
	v_cvt_pk_bf16_f32 v27, v28, v29
	ds_read_b128 v[28:31], v33 offset:20480
	ds_read_b128 v[68:71], v64 offset:20480
	ds_read_b128 v[72:75], v66 offset:832
	s_waitcnt lgkmcnt(2)
	v_mfma_f32_16x16x32_bf16 v[28:31], v[28:31], v[2:5], 0
	ds_read_b128 v[76:79], v63 offset:20480
	v_cmp_le_i32_e32 vcc, v67, v32
	s_waitcnt lgkmcnt(2)
	v_mfma_f32_16x16x32_bf16 v[28:31], v[68:71], v[6:9], v[28:31]
	ds_read_b128 v[68:71], v65 offset:20480
	s_waitcnt lgkmcnt(1)
	v_mfma_f32_16x16x32_bf16 v[28:31], v[76:79], v[10:13], v[28:31]
	s_waitcnt lgkmcnt(0)
	v_mfma_f32_16x16x32_bf16 v[28:31], v[68:71], v[14:17], v[28:31]
	v_sub_f32_e32 v69, v72, v82
	v_min_f32_e32 v69, 0, v69
	v_mul_f32_e32 v69, 0x3fb8aa3b, v69
	v_exp_f32_e32 v69, v69
	v_cndmask_b32_e64 v68, 0, 1, vcc
	v_cmp_ge_i32_e32 vcc, v67, v32
	s_nop 1
	v_mul_f32_e32 v28, v28, v69
	v_cndmask_b32_e64 v67, 0, 1, vcc
	v_sub_f32_e32 v69, v73, v82
	v_cndmask_b32_e64 v67, v67, v68, s[44:45]
	v_min_f32_e32 v69, 0, v69
	v_and_b32_e32 v67, 1, v67
	v_mul_f32_e32 v69, 0x3fb8aa3b, v69
	v_cmp_eq_u32_e32 vcc, 1, v67
	v_add_u32_e32 v67, 0x51, v50
	v_exp_f32_e32 v69, v69
	v_cndmask_b32_e32 v28, 0, v28, vcc
	v_cmp_le_i32_e32 vcc, v67, v32
	v_mul_f32_e32 v29, v29, v69
	s_nop 0
	v_cndmask_b32_e64 v68, 0, 1, vcc
	v_cmp_ge_i32_e32 vcc, v67, v32
	v_sub_f32_e32 v69, v74, v82
	v_min_f32_e32 v69, 0, v69
	v_cndmask_b32_e64 v67, 0, 1, vcc
	v_cndmask_b32_e64 v67, v67, v68, s[44:45]
	v_and_b32_e32 v67, 1, v67
	v_cmp_eq_u32_e32 vcc, 1, v67
	v_add_u32_e32 v67, 0x52, v50
	v_mul_f32_e32 v69, 0x3fb8aa3b, v69
	v_cndmask_b32_e32 v29, 0, v29, vcc
	v_cmp_le_i32_e32 vcc, v67, v32
	v_exp_f32_e32 v69, v69
	v_cvt_pk_bf16_f32 v28, v28, v29
	s_nop 0
	v_cndmask_b32_e64 v68, 0, 1, vcc
	v_cmp_ge_i32_e32 vcc, v67, v32
	v_mul_f32_e32 v30, v30, v69
	v_sub_f32_e32 v69, v75, v82
	v_cndmask_b32_e64 v67, 0, 1, vcc
	v_cndmask_b32_e64 v67, v67, v68, s[44:45]
	v_and_b32_e32 v67, 1, v67
	v_cmp_eq_u32_e32 vcc, 1, v67
	v_add_u32_e32 v67, 0x53, v50
	v_min_f32_e32 v69, 0, v69
	v_cndmask_b32_e32 v30, 0, v30, vcc
	v_cmp_le_i32_e32 vcc, v67, v32
	v_mul_f32_e32 v69, 0x3fb8aa3b, v69
	v_exp_f32_e32 v69, v69
	v_cndmask_b32_e64 v68, 0, 1, vcc
	v_cmp_ge_i32_e32 vcc, v67, v32
	v_mul_f32_e32 v31, v31, v69
	s_nop 0
	v_cndmask_b32_e64 v67, 0, 1, vcc
	v_cndmask_b32_e64 v67, v67, v68, s[44:45]
	v_and_b32_e32 v67, 1, v67
	v_cmp_eq_u32_e32 vcc, 1, v67
	s_nop 1
	v_cndmask_b32_e32 v31, 0, v31, vcc
	v_cvt_pk_bf16_f32 v29, v30, v31
	ds_read_b128 v[68:71], v33 offset:24576
	ds_read_b128 v[72:75], v64 offset:24576
	ds_read_b128 v[76:79], v66 offset:896
	s_waitcnt lgkmcnt(2)
	v_mfma_f32_16x16x32_bf16 v[68:71], v[68:71], v[2:5], 0
	ds_read_b128 v[218:221], v63 offset:24576
	s_waitcnt lgkmcnt(1)
	v_sub_f32_e32 v67, v76, v82
	v_add_u32_e32 v30, 0x60, v50
	v_mfma_f32_16x16x32_bf16 v[68:71], v[72:75], v[6:9], v[68:71]
	ds_read_b128 v[72:75], v65 offset:24576
	v_min_f32_e32 v67, 0, v67
	v_cmp_le_i32_e32 vcc, v30, v32
	s_waitcnt lgkmcnt(1)
	v_mfma_f32_16x16x32_bf16 v[68:71], v[218:221], v[10:13], v[68:71]
	v_mul_f32_e32 v67, 0x3fb8aa3b, v67
	v_cndmask_b32_e64 v31, 0, 1, vcc
	v_exp_f32_e32 v67, v67
	s_waitcnt lgkmcnt(0)
	v_mfma_f32_16x16x32_bf16 v[68:71], v[72:75], v[14:17], v[68:71]
	v_cmp_ge_i32_e32 vcc, v30, v32
	s_nop 1
	v_cndmask_b32_e64 v30, 0, 1, vcc
	v_cndmask_b32_e64 v30, v30, v31, s[44:45]
	v_and_b32_e32 v30, 1, v30
	s_nop 1
	v_mul_f32_e32 v31, v68, v67
	v_cmp_eq_u32_e32 vcc, 1, v30
	v_sub_f32_e32 v68, v77, v82
	v_min_f32_e32 v68, 0, v68
	v_cndmask_b32_e32 v30, 0, v31, vcc
	v_add_u32_e32 v31, 0x61, v50
	v_cmp_le_i32_e32 vcc, v31, v32
	v_mul_f32_e32 v68, 0x3fb8aa3b, v68
	v_exp_f32_e32 v68, v68
	v_cndmask_b32_e64 v67, 0, 1, vcc
	v_cmp_ge_i32_e32 vcc, v31, v32
	s_nop 1
	v_cndmask_b32_e64 v31, 0, 1, vcc
	v_cndmask_b32_e64 v31, v31, v67, s[44:45]
	v_and_b32_e32 v31, 1, v31
	v_mul_f32_e32 v67, v69, v68
	v_cmp_eq_u32_e32 vcc, 1, v31
	v_sub_f32_e32 v69, v78, v82
	v_min_f32_e32 v69, 0, v69
	v_cndmask_b32_e32 v31, 0, v67, vcc
	v_add_u32_e32 v67, 0x62, v50
	v_cmp_le_i32_e32 vcc, v67, v32
	v_mul_f32_e32 v69, 0x3fb8aa3b, v69
	v_exp_f32_e32 v69, v69
	v_cndmask_b32_e64 v68, 0, 1, vcc
	v_cmp_ge_i32_e32 vcc, v67, v32
	v_cvt_pk_bf16_f32 v30, v30, v31
	s_nop 1
	v_cndmask_b32_e64 v67, 0, 1, vcc
	v_cndmask_b32_e64 v67, v67, v68, s[44:45]
	v_and_b32_e32 v67, 1, v67
	v_mul_f32_e32 v68, v70, v69
	v_cmp_eq_u32_e32 vcc, 1, v67
	v_sub_f32_e32 v70, v79, v82
	v_min_f32_e32 v70, 0, v70
	v_cndmask_b32_e32 v67, 0, v68, vcc
	v_add_u32_e32 v68, 0x63, v50
	v_cmp_le_i32_e32 vcc, v68, v32
	v_mul_f32_e32 v70, 0x3fb8aa3b, v70
	v_exp_f32_e32 v70, v70
	v_cndmask_b32_e64 v69, 0, 1, vcc
	v_cmp_ge_i32_e32 vcc, v68, v32
	s_nop 1
	v_cndmask_b32_e64 v68, 0, 1, vcc
	v_cndmask_b32_e64 v68, v68, v69, s[44:45]
	v_and_b32_e32 v68, 1, v68
	v_mul_f32_e32 v69, v71, v70
	v_cmp_eq_u32_e32 vcc, 1, v68
	s_nop 1
	v_cndmask_b32_e32 v68, 0, v69, vcc
	v_cvt_pk_bf16_f32 v31, v67, v68
	ds_read_b128 v[68:71], v33 offset:28672
	ds_read_b128 v[72:75], v64 offset:28672
	ds_read_b128 v[76:79], v66 offset:960
	s_waitcnt lgkmcnt(2)
	v_mfma_f32_16x16x32_bf16 v[66:69], v[68:71], v[2:5], 0
	ds_read_b128 v[218:221], v63 offset:28672
	v_add_u32_e32 v33, 0x70, v50
	v_cmp_le_i32_e32 vcc, v33, v32
	s_waitcnt lgkmcnt(2)
	v_mfma_f32_16x16x32_bf16 v[66:69], v[72:75], v[6:9], v[66:69]
	ds_read_b128 v[70:73], v65 offset:28672
	v_cndmask_b32_e64 v63, 0, 1, vcc
	v_cmp_ge_i32_e32 vcc, v33, v32
	s_waitcnt lgkmcnt(1)
	v_mfma_f32_16x16x32_bf16 v[66:69], v[218:221], v[10:13], v[66:69]
	v_cndmask_b32_e64 v33, 0, 1, vcc
	v_cndmask_b32_e64 v33, v33, v63, s[44:45]
	v_and_b32_e32 v33, 1, v33
	s_waitcnt lgkmcnt(0)
	v_mfma_f32_16x16x32_bf16 v[64:67], v[70:73], v[14:17], v[66:69]
	v_cmp_eq_u32_e32 vcc, 1, v33
	s_nop 1
	v_sub_f32_e32 v68, v76, v82
	v_min_f32_e32 v68, 0, v68
	v_mul_f32_e32 v68, 0x3fb8aa3b, v68
	v_exp_f32_e32 v68, v68
	s_nop 0
	v_mul_f32_e32 v63, v64, v68
	v_sub_f32_e32 v68, v77, v82
	v_cndmask_b32_e32 v33, 0, v63, vcc
	v_add_u32_e32 v63, 0x71, v50
	v_min_f32_e32 v68, 0, v68
	v_cmp_le_i32_e32 vcc, v63, v32
	v_mul_f32_e32 v68, 0x3fb8aa3b, v68
	v_exp_f32_e32 v68, v68
	v_cndmask_b32_e64 v64, 0, 1, vcc
	v_cmp_ge_i32_e32 vcc, v63, v32
	s_nop 1
	v_cndmask_b32_e64 v63, 0, 1, vcc
	v_cndmask_b32_e64 v63, v63, v64, s[44:45]
	v_and_b32_e32 v63, 1, v63
	v_mul_f32_e32 v64, v65, v68
	v_cmp_eq_u32_e32 vcc, 1, v63
	v_sub_f32_e32 v68, v78, v82
	v_min_f32_e32 v68, 0, v68
	v_cndmask_b32_e32 v63, 0, v64, vcc
	v_add_u32_e32 v64, 0x72, v50
	v_cmp_le_i32_e32 vcc, v64, v32
	v_mul_f32_e32 v68, 0x3fb8aa3b, v68
	v_exp_f32_e32 v68, v68
	v_cndmask_b32_e64 v65, 0, 1, vcc
	v_cmp_ge_i32_e32 vcc, v64, v32
	s_nop 1
	v_cndmask_b32_e64 v64, 0, 1, vcc
	v_cndmask_b32_e64 v64, v64, v65, s[44:45]
	v_and_b32_e32 v64, 1, v64
	v_mul_f32_e32 v65, v66, v68
	v_cmp_eq_u32_e32 vcc, 1, v64
	v_sub_f32_e32 v68, v79, v82
	v_min_f32_e32 v68, 0, v68
	v_cndmask_b32_e32 v64, 0, v65, vcc
	v_add_u32_e32 v65, 0x73, v50
	v_cmp_le_i32_e32 vcc, v65, v32
	v_mul_f32_e32 v68, 0x3fb8aa3b, v68
	v_exp_f32_e32 v68, v68
	v_cndmask_b32_e64 v66, 0, 1, vcc
	v_cmp_ge_i32_e32 vcc, v65, v32
	v_mul_f32_e32 v65, v67, v68
	s_nop 0
	v_cndmask_b32_e64 v32, 0, 1, vcc
	v_cndmask_b32_e64 v32, v32, v66, s[44:45]
	v_and_b32_e32 v32, 1, v32
	v_cmp_eq_u32_e32 vcc, 1, v32
	v_cvt_pk_bf16_f32 v32, v33, v63
	s_nop 1
	v_cndmask_b32_e32 v65, 0, v65, vcc
	v_cvt_pk_bf16_f32 v33, v64, v65
	v_lshlrev_b32_e32 v64, 3, v53
	v_mov_b32_e32 v65, v87
	v_lshl_add_u64 v[68:69], v[64:65], 1, s[48:49]
	v_add_co_u32_e32 v64, vcc, s59, v68
	v_lshl_add_u64 v[76:77], v[68:69], 0, s[42:43]
	s_nop 0
	v_addc_co_u32_e32 v65, vcc, 0, v69, vcc
	global_load_dwordx4 v[64:67], v[64:65], off
	s_nop 0
	global_load_dwordx4 v[68:71], v[76:77], off offset:64
	global_load_dwordx4 v[72:75], v[76:77], off offset:128
	s_nop 0
	global_load_dwordx4 v[76:79], v[76:77], off offset:192
	v_cmp_eq_u32_e32 vcc, 0, v56
	ds_read_b32 v83, v62
	s_nop 0
	v_cndmask_b32_e32 v63, 0, v200, vcc
	s_waitcnt vmcnt(2)
	v_cndmask_b32_e32 v71, 0, v71, vcc
	v_cndmask_b32_e32 v67, 0, v67, vcc
	v_cndmask_b32_e32 v66, 0, v66, vcc
	v_cndmask_b32_e32 v65, 0, v65, vcc
	v_cndmask_b32_e32 v64, 0, v64, vcc
	v_cndmask_b32_e32 v70, 0, v70, vcc
	v_cndmask_b32_e32 v69, 0, v69, vcc
	v_cndmask_b32_e32 v68, 0, v68, vcc
	v_mfma_f32_16x16x32_bf16 v[64:67], v[64:67], v[2:5], 0
	s_nop 0
	v_mfma_f32_16x16x32_bf16 v[64:67], v[68:71], v[6:9], v[64:67]
	s_waitcnt vmcnt(1)
	v_cndmask_b32_e32 v71, 0, v75, vcc
	v_cndmask_b32_e32 v70, 0, v74, vcc
	v_cndmask_b32_e32 v69, 0, v73, vcc
	v_cndmask_b32_e32 v68, 0, v72, vcc
	s_nop 1
	v_mfma_f32_16x16x32_bf16 v[64:67], v[68:71], v[10:13], v[64:67]
	s_waitcnt vmcnt(0)
	v_cndmask_b32_e32 v71, 0, v79, vcc
	v_cndmask_b32_e32 v70, 0, v78, vcc
	v_cndmask_b32_e32 v69, 0, v77, vcc
	v_cndmask_b32_e32 v68, 0, v76, vcc
	s_andn2_b64 vcc, exec, s[46:47]
	s_nop 0
	v_mfma_f32_16x16x32_bf16 v[64:67], v[68:71], v[14:17], v[64:67]
	v_perm_b32 v68, v63, v63, s73
	v_mov_b32_e32 v69, v68
	v_mov_b32_e32 v70, v68
	v_mov_b32_e32 v71, v68
	s_nop 3
	v_mul_f32_e32 v64, v180, v64
	s_nop 1
	v_mfma_f32_16x16x32_bf16 v[64:67], v[68:71], v[18:21], v[64:67]
	v_mfma_f32_16x16x32_bf16 v[64:67], v[68:71], v[22:25], v[64:67]
	v_mfma_f32_16x16x32_bf16 v[64:67], v[68:71], v[26:29], v[64:67]
	v_mfma_f32_16x16x32_bf16 v[62:65], v[68:71], v[30:33], v[64:67]
	s_nop 7
	ds_bpermute_b32 v107, v51, v62
	s_cbranch_vccnz .LBB0_775
	v_or_b32_e32 v62, s81, v56
	v_mov_b32_e32 v63, s82
	v_lshlrev_b64 v[62:63], 11, v[62:63]
	v_lshl_add_u64 v[62:63], s[0:1], 0, v[62:63]
	v_mov_b32_e32 v51, v87
	v_lshl_add_u64 v[50:51], v[62:63], 0, v[50:51]
	v_lshrrev_b32_e32 v105, 4, v230
	v_mad_u64_u32 v[50:51], s[100:101], v105, 12, v[50:51]
	global_load_dwordx4 v[204:207], v[50:51], off
	global_load_dwordx4 v[208:211], v[50:51], off offset:64
	global_load_dwordx4 v[212:215], v[50:51], off offset:128
	global_load_dwordx2 v[202:203], v[50:51], off offset:192
	global_load_dwordx2 v[216:217], v[50:51], off offset:200
	s_branch .LBB0_775

	.amdhsa_kernel _Z6mk_fwd4Args
		.amdhsa_group_segment_fixed_size 0
		.amdhsa_private_segment_fixed_size 0
		.amdhsa_kernarg_size 488
		.amdhsa_user_sgpr_count 2
		.amdhsa_user_sgpr_dispatch_ptr 0
		.amdhsa_user_sgpr_queue_ptr 0
		.amdhsa_user_sgpr_kernarg_segment_ptr 1
		.amdhsa_user_sgpr_dispatch_id 0
		.amdhsa_user_sgpr_kernarg_preload_length 0
		.amdhsa_user_sgpr_kernarg_preload_offset 0
		.amdhsa_user_sgpr_private_segment_size 0
		.amdhsa_uses_dynamic_stack 0
		.amdhsa_enable_private_segment 0
		.amdhsa_system_sgpr_workgroup_id_x 1
		.amdhsa_system_sgpr_workgroup_id_y 0
		.amdhsa_system_sgpr_workgroup_id_z 0
		.amdhsa_system_sgpr_workgroup_info 0
		.amdhsa_system_vgpr_workitem_id 0
		.amdhsa_next_free_vgpr 253
		.amdhsa_next_free_sgpr 102
		.amdhsa_accum_offset 256
		.amdhsa_reserve_vcc 1
		.amdhsa_float_round_mode_32 0
		.amdhsa_float_round_mode_16_64 0
		.amdhsa_float_denorm_mode_32 3
		.amdhsa_float_denorm_mode_16_64 3
		.amdhsa_dx10_clamp 1
		.amdhsa_ieee_mode 1
		.amdhsa_fp16_overflow 0
		.amdhsa_tg_split 0
		.amdhsa_exception_fp_ieee_invalid_op 0
		.amdhsa_exception_fp_denorm_src 0
		.amdhsa_exception_fp_ieee_div_zero 0
		.amdhsa_exception_fp_ieee_overflow 0
		.amdhsa_exception_fp_ieee_underflow 0
		.amdhsa_exception_fp_ieee_inexact 0
		.amdhsa_exception_int_div_zero 0
	.end_amdhsa_kernel

amdhsa.kernels:
  - .agpr_count:     0
    .args:
      - .offset:         0
        .size:           232
        .value_kind:     by_value
      - .offset:         232
        .size:           4
        .value_kind:     hidden_block_count_x
      - .offset:         236
        .size:           4
        .value_kind:     hidden_block_count_y
      - .offset:         240
        .size:           4
        .value_kind:     hidden_block_count_z
      - .offset:         244
        .size:           2
        .value_kind:     hidden_group_size_x
      - .offset:         246
        .size:           2
        .value_kind:     hidden_group_size_y
      - .offset:         248
        .size:           2
        .value_kind:     hidden_group_size_z
      - .offset:         250
        .size:           2
        .value_kind:     hidden_remainder_x
      - .offset:         252
        .size:           2
        .value_kind:     hidden_remainder_y
      - .offset:         254
        .size:           2
        .value_kind:     hidden_remainder_z
      - .offset:         272
        .size:           8
        .value_kind:     hidden_global_offset_x
      - .offset:         280
        .size:           8
        .value_kind:     hidden_global_offset_y
      - .offset:         288
        .size:           8
        .value_kind:     hidden_global_offset_z
      - .offset:         296
        .size:           2
        .value_kind:     hidden_grid_dims
      - .offset:         352
        .size:           4
        .value_kind:     hidden_dynamic_lds_size
    .group_segment_fixed_size: 0
    .kernarg_segment_align: 8
    .kernarg_segment_size: 488
    .language:       OpenCL C
    .language_version:
      - 2
      - 0
    .max_flat_workgroup_size: 512
    .name:           _Z6mk_fwd4Args
    .private_segment_fixed_size: 0
    .sgpr_count:     108
    .sgpr_spill_count: 6
    .symbol:         _Z6mk_fwd4Args.kd
    .uniform_work_group_size: 1
    .uses_dynamic_stack: false
    .vgpr_count:     253
    .vgpr_spill_count: 0
    .wavefront_size: 64
